# S1 + SwiGLU epilogues (MoE and dense gate/up): sigmoid chains interleaved on renamed temporaries by a hazard-aware list scheduler, 163 s_nop removed; dataflow checked symbolically
# speedup vs baseline: 1.0013x; 1.0013x over previous
.LBB0_1312:
	v_cvt_f32_i32_e32 v124, v124
	v_cvt_f32_i32_e32 v125, v125
	v_cvt_f32_i32_e32 v140, v88
	v_cvt_f32_i32_e32 v88, v86
	v_cvt_f32_i32_e32 v86, v80
	v_cvt_f32_i32_e32 v80, v78
	v_cvt_f32_i32_e32 v78, v72
	v_cvt_f32_i32_e32 v72, v70
	v_cvt_f32_i32_e32 v70, v64
	v_cvt_f32_i32_e32 v64, v60
	v_cvt_f32_i32_e32 v60, v56
	v_cvt_f32_i32_e32 v56, v52
	v_cvt_f32_i32_e32 v52, v48
	v_cvt_f32_i32_e32 v48, v44
	v_cvt_f32_i32_e32 v44, v40
	v_cvt_f32_i32_e32 v40, v36
	v_cvt_f32_i32_e32 v36, v32
	v_cvt_f32_i32_e32 v32, v34
	v_cvt_f32_i32_e32 v34, v30
	v_cvt_f32_i32_e32 v30, v24
	v_cvt_f32_i32_e32 v24, v22
	v_cvt_f32_i32_e32 v22, v16
	v_cvt_f32_i32_e32 v16, v14
	v_cvt_f32_i32_e32 v14, v8
	v_cvt_f32_i32_e32 v8, v4
	v_cvt_f32_i32_e32 v4, v0
	v_mbcnt_lo_u32_b32 v0, -1, 0
	v_mbcnt_hi_u32_b32 v0, -1, v0
	s_lshl_b32 s9, s52, 8
	v_cvt_f32_i32_e32 v141, v89
	v_cvt_f32_i32_e32 v89, v87
	v_cvt_f32_i32_e32 v87, v81
	v_cvt_f32_i32_e32 v81, v79
	v_cvt_f32_i32_e32 v79, v73
	v_cvt_f32_i32_e32 v73, v71
	v_cvt_f32_i32_e32 v71, v65
	v_cvt_f32_i32_e32 v65, v61
	v_cvt_f32_i32_e32 v61, v57
	v_cvt_f32_i32_e32 v57, v53
	v_cvt_f32_i32_e32 v53, v49
	v_cvt_f32_i32_e32 v49, v45
	v_cvt_f32_i32_e32 v45, v41
	v_cvt_f32_i32_e32 v41, v37
	v_cvt_f32_i32_e32 v37, v33
	v_cvt_f32_i32_e32 v33, v35
	v_cvt_f32_i32_e32 v35, v31
	v_cvt_f32_i32_e32 v31, v25
	v_cvt_f32_i32_e32 v25, v23
	v_cvt_f32_i32_e32 v23, v17
	v_cvt_f32_i32_e32 v17, v15
	v_cvt_f32_i32_e32 v15, v9
	v_cvt_f32_i32_e32 v9, v5
	v_cvt_f32_i32_e32 v5, v1
	s_add_i32 s9, s9, s69
	v_ashrrev_i32_e32 v1, 2, v0
	v_cvt_f32_i32_e32 v139, v121
	v_cvt_f32_i32_e32 v121, v117
	v_cvt_f32_i32_e32 v117, v113
	v_cvt_f32_i32_e32 v113, v109
	v_cvt_f32_i32_e32 v109, v105
	v_cvt_f32_i32_e32 v105, v101
	v_cvt_f32_i32_e32 v101, v97
	v_cvt_f32_i32_e32 v97, v99
	v_cvt_f32_i32_e32 v99, v93
	v_cvt_f32_i32_e32 v142, v90
	v_cvt_f32_i32_e32 v90, v84
	v_cvt_f32_i32_e32 v84, v82
	v_cvt_f32_i32_e32 v82, v76
	v_cvt_f32_i32_e32 v76, v74
	v_cvt_f32_i32_e32 v74, v68
	v_cvt_f32_i32_e32 v68, v66
	v_cvt_f32_i32_e32 v66, v28
	v_cvt_f32_i32_e32 v28, v26
	v_cvt_f32_i32_e32 v26, v20
	v_cvt_f32_i32_e32 v20, v18
	v_cvt_f32_i32_e32 v18, v12
	v_cvt_f32_i32_e32 v12, v10
	v_and_b32_e32 v10, 3, v0
	v_and_b32_e32 v0, -4, v0
	v_add_u32_e32 v93, s9, v1
	s_lshl_b32 s9, s85, 7
	v_cvt_f32_i32_e32 v138, v120
	v_cvt_f32_i32_e32 v120, v116
	v_cvt_f32_i32_e32 v116, v112
	v_cvt_f32_i32_e32 v112, v108
	v_cvt_f32_i32_e32 v108, v104
	v_cvt_f32_i32_e32 v104, v100
	v_cvt_f32_i32_e32 v100, v96
	v_cvt_f32_i32_e32 v96, v98
	v_cvt_f32_i32_e32 v98, v92
	v_cvt_f32_i32_e32 v143, v91
	v_cvt_f32_i32_e32 v91, v85
	v_cvt_f32_i32_e32 v85, v83
	v_cvt_f32_i32_e32 v83, v77
	v_cvt_f32_i32_e32 v77, v75
	v_cvt_f32_i32_e32 v75, v69
	v_cvt_f32_i32_e32 v69, v67
	v_cvt_f32_i32_e32 v67, v29
	v_cvt_f32_i32_e32 v29, v27
	v_cvt_f32_i32_e32 v27, v21
	v_cvt_f32_i32_e32 v21, v19
	v_cvt_f32_i32_e32 v19, v13
	v_cvt_f32_i32_e32 v13, v11
	v_lshl_add_u32 v92, v10, 6, v0
	v_lshl_or_b32 v0, v10, 3, s9
	v_pk_mul_f32 v[10:11], v[128:129], v[124:125]
	v_cvt_f32_i32_e32 v126, v126
	v_exp_f32_e32 v10, v10
	v_exp_f32_e32 v11, v11
	v_cvt_f32_i32_e32 v127, v127
	v_pk_mul_f32 v[124:125], v[130:131], v[124:125]
	v_cvt_f32_i32_e32 v94, v94
	v_pk_add_f32 v[10:11], v[10:11], 1.0 op_sel_hi:[1,0]
	v_pk_mul_f32 v[98:99], v[124:125], v[98:99]
	v_rcp_f32_e32 v10, v10
	v_rcp_f32_e32 v11, v11
	v_cvt_f32_i32_e32 v95, v95
	v_pk_mul_f32 v[124:125], v[130:131], v[126:127]
	v_cvt_f32_i32_e32 v122, v122
	v_pk_mul_f32 v[10:11], v[10:11], v[98:99]
	v_pk_mul_f32 v[206:207], v[128:129], v[126:127]
	v_pk_mul_f32 v[94:95], v[124:125], v[94:95]
	v_exp_f32_e32 v206, v206
	v_exp_f32_e32 v207, v207
	v_cvt_f32_i32_e32 v123, v123
	v_pk_mul_f32 v[208:209], v[130:131], v[138:139]
	v_or_b32_e32 v0, s70, v0
	v_pk_add_f32 v[206:207], v[206:207], 1.0 op_sel_hi:[1,0]
	v_pk_mul_f32 v[208:209], v[208:209], v[140:141]
	v_rcp_f32_e32 v206, v206
	v_rcp_f32_e32 v207, v207
	s_movk_i32 s9, 0x1c00
	v_ashrrev_i32_e32 v1, 31, v0
	v_cvt_f32_i32_e32 v118, v118
	v_pk_mul_f32 v[94:95], v[206:207], v[94:95]
	v_pk_mul_f32 v[98:99], v[128:129], v[138:139]
	v_cvt_f32_i32_e32 v119, v119
	v_exp_f32_e32 v98, v98
	v_exp_f32_e32 v99, v99
	v_cvt_f32_i32_e32 v114, v114
	v_cvt_f32_i32_e32 v115, v115
	v_cvt_f32_i32_e32 v110, v110
	v_pk_add_f32 v[98:99], v[98:99], 1.0 op_sel_hi:[1,0]
	v_cvt_f32_i32_e32 v111, v111
	v_rcp_f32_e32 v98, v98
	v_rcp_f32_e32 v99, v99
	v_cvt_f32_i32_e32 v106, v106
	v_cvt_f32_i32_e32 v107, v107
	v_cvt_f32_i32_e32 v102, v102
	v_pk_mul_f32 v[98:99], v[98:99], v[208:209]
	v_pk_mul_f32 v[124:125], v[128:129], v[122:123]
	v_pk_mul_f32 v[122:123], v[130:131], v[122:123]
	v_exp_f32_e32 v124, v124
	v_exp_f32_e32 v125, v125
	v_pk_mul_f32 v[122:123], v[122:123], v[142:143]
	v_cvt_f32_i32_e32 v103, v103
	v_cvt_f32_i32_e32 v62, v62
	v_pk_add_f32 v[124:125], v[124:125], 1.0 op_sel_hi:[1,0]
	v_cvt_f32_i32_e32 v63, v63
	v_rcp_f32_e32 v124, v124
	v_rcp_f32_e32 v125, v125
	v_cvt_f32_i32_e32 v58, v58
	v_cvt_f32_i32_e32 v59, v59
	v_cvt_f32_i32_e32 v54, v54
	v_pk_mul_f32 v[122:123], v[124:125], v[122:123]
	v_cvt_pk_fp8_f32 v124, v10, v11
	v_cvt_pk_fp8_f32 v10, v98, v99
	v_cvt_f32_i32_e32 v55, v55
	v_cvt_pk_fp8_f32 v124, v94, v95 op_sel:[0,0,1]
	v_cvt_f32_i32_e32 v50, v50
	v_cvt_pk_fp8_f32 v10, v122, v123 op_sel:[0,0,1]
	v_cvt_f32_i32_e32 v51, v51
	ds_bpermute_b32 v94, v92, v124
	v_cvt_f32_i32_e32 v46, v46
	ds_bpermute_b32 v95, v92, v10
	v_mov_b64_e32 v[10:11], s[22:23]
	v_mad_i64_i32 v[98:99], s[10:11], v93, s9, v[10:11]
	v_lshl_add_u64 v[98:99], v[98:99], 0, v[0:1]
	s_waitcnt lgkmcnt(0)
	global_store_dwordx2 v[98:99], v[94:95], off
	v_pk_mul_f32 v[94:95], v[128:129], v[118:119]
	v_pk_mul_f32 v[206:207], v[128:129], v[120:121]
	v_exp_f32_e32 v94, v94
	v_exp_f32_e32 v95, v95
	v_exp_f32_e32 v206, v206
	v_exp_f32_e32 v207, v207
	v_pk_add_f32 v[94:95], v[94:95], 1.0 op_sel_hi:[1,0]
	v_pk_mul_f32 v[98:99], v[130:131], v[118:119]
	v_pk_add_f32 v[206:207], v[206:207], 1.0 op_sel_hi:[1,0]
	v_pk_mul_f32 v[208:209], v[130:131], v[120:121]
	v_rcp_f32_e32 v94, v94
	v_rcp_f32_e32 v95, v95
	v_pk_mul_f32 v[88:89], v[98:99], v[88:89]
	v_rcp_f32_e32 v206, v206
	v_rcp_f32_e32 v207, v207
	v_pk_mul_f32 v[90:91], v[208:209], v[90:91]
	v_pk_mul_f32 v[88:89], v[94:95], v[88:89]
	v_pk_mul_f32 v[90:91], v[206:207], v[90:91]
	v_pk_mul_f32 v[94:95], v[128:129], v[114:115]
	v_pk_mul_f32 v[206:207], v[128:129], v[116:117]
	v_exp_f32_e32 v94, v94
	v_exp_f32_e32 v95, v95
	v_exp_f32_e32 v206, v206
	v_exp_f32_e32 v207, v207
	v_pk_add_f32 v[94:95], v[94:95], 1.0 op_sel_hi:[1,0]
	v_pk_mul_f32 v[98:99], v[130:131], v[114:115]
	v_pk_add_f32 v[206:207], v[206:207], 1.0 op_sel_hi:[1,0]
	v_pk_mul_f32 v[208:209], v[130:131], v[116:117]
	v_rcp_f32_e32 v94, v94
	v_rcp_f32_e32 v95, v95
	v_pk_mul_f32 v[84:85], v[98:99], v[84:85]
	v_rcp_f32_e32 v206, v206
	v_rcp_f32_e32 v207, v207
	v_pk_mul_f32 v[86:87], v[208:209], v[86:87]
	v_pk_mul_f32 v[84:85], v[94:95], v[84:85]
	v_pk_mul_f32 v[86:87], v[206:207], v[86:87]
	v_cvt_pk_fp8_f32 v94, v90, v91
	v_cvt_pk_fp8_f32 v94, v88, v89 op_sel:[0,0,1]
	v_cvt_f32_i32_e32 v47, v47
	v_cvt_f32_i32_e32 v42, v42
	v_cvt_f32_i32_e32 v43, v43
	v_cvt_f32_i32_e32 v38, v38
	v_cvt_f32_i32_e32 v39, v39
	v_cvt_f32_i32_e32 v6, v6
	v_cvt_f32_i32_e32 v7, v7
	v_cvt_f32_i32_e32 v2, v2
	v_cvt_f32_i32_e32 v3, v3
	s_mov_b64 s[52:53], -1
	s_andn2_b64 vcc, exec, s[44:45]
	v_readlane_b32 s90, v255, 39
	v_readlane_b32 s91, v255, 40
	v_cvt_pk_fp8_f32 v89, v86, v87
	v_pk_mul_f32 v[206:207], v[130:131], v[112:113]
	ds_bpermute_b32 v88, v92, v94
	v_pk_mul_f32 v[82:83], v[206:207], v[82:83]
	v_cvt_pk_fp8_f32 v89, v84, v85 op_sel:[0,0,1]
	v_add_u32_e32 v84, 16, v93
	v_mad_i64_i32 v[84:85], s[10:11], v84, s9, v[10:11]
	ds_bpermute_b32 v89, v92, v89
	v_lshl_add_u64 v[84:85], v[84:85], 0, v[0:1]
	v_pk_mul_f32 v[86:87], v[130:131], v[110:111]
	s_waitcnt lgkmcnt(0)
	global_store_dwordx2 v[84:85], v[88:89], off
	v_pk_mul_f32 v[84:85], v[128:129], v[110:111]
	v_pk_mul_f32 v[206:207], v[128:129], v[112:113]
	v_exp_f32_e32 v84, v84
	v_exp_f32_e32 v85, v85
	v_exp_f32_e32 v206, v206
	v_exp_f32_e32 v207, v207
	v_pk_add_f32 v[84:85], v[84:85], 1.0 op_sel_hi:[1,0]
	v_pk_add_f32 v[206:207], v[206:207], 1.0 op_sel_hi:[1,0]
	v_rcp_f32_e32 v84, v84
	v_rcp_f32_e32 v85, v85
	v_pk_mul_f32 v[80:81], v[86:87], v[80:81]
	v_rcp_f32_e32 v206, v206
	v_rcp_f32_e32 v207, v207
	v_pk_mul_f32 v[80:81], v[84:85], v[80:81]
	v_pk_mul_f32 v[82:83], v[206:207], v[82:83]
	v_pk_mul_f32 v[84:85], v[128:129], v[106:107]
	v_pk_mul_f32 v[206:207], v[128:129], v[108:109]
	v_exp_f32_e32 v84, v84
	v_exp_f32_e32 v85, v85
	v_exp_f32_e32 v206, v206
	v_exp_f32_e32 v207, v207
	v_pk_add_f32 v[84:85], v[84:85], 1.0 op_sel_hi:[1,0]
	v_pk_mul_f32 v[86:87], v[130:131], v[106:107]
	v_pk_add_f32 v[206:207], v[206:207], 1.0 op_sel_hi:[1,0]
	v_pk_mul_f32 v[208:209], v[130:131], v[108:109]
	v_rcp_f32_e32 v84, v84
	v_rcp_f32_e32 v85, v85
	v_pk_mul_f32 v[76:77], v[86:87], v[76:77]
	v_rcp_f32_e32 v206, v206
	v_rcp_f32_e32 v207, v207
	v_pk_mul_f32 v[78:79], v[208:209], v[78:79]
	v_pk_mul_f32 v[76:77], v[84:85], v[76:77]
	v_pk_mul_f32 v[78:79], v[206:207], v[78:79]
	v_cvt_pk_fp8_f32 v84, v82, v83
	v_cvt_pk_fp8_f32 v84, v80, v81 op_sel:[0,0,1]
	v_cvt_pk_fp8_f32 v81, v78, v79
	v_pk_mul_f32 v[206:207], v[130:131], v[104:105]
	ds_bpermute_b32 v80, v92, v84
	v_pk_mul_f32 v[74:75], v[206:207], v[74:75]
	v_cvt_pk_fp8_f32 v81, v76, v77 op_sel:[0,0,1]
	v_add_u32_e32 v76, 32, v93
	v_mad_i64_i32 v[76:77], s[10:11], v76, s9, v[10:11]
	ds_bpermute_b32 v81, v92, v81
	v_lshl_add_u64 v[76:77], v[76:77], 0, v[0:1]
	v_pk_mul_f32 v[78:79], v[130:131], v[102:103]
	s_waitcnt lgkmcnt(0)
	global_store_dwordx2 v[76:77], v[80:81], off
	v_pk_mul_f32 v[76:77], v[128:129], v[102:103]
	v_pk_mul_f32 v[206:207], v[128:129], v[104:105]
	v_exp_f32_e32 v76, v76
	v_exp_f32_e32 v77, v77
	v_exp_f32_e32 v206, v206
	v_exp_f32_e32 v207, v207
	v_pk_add_f32 v[76:77], v[76:77], 1.0 op_sel_hi:[1,0]
	v_pk_add_f32 v[206:207], v[206:207], 1.0 op_sel_hi:[1,0]
	v_rcp_f32_e32 v76, v76
	v_rcp_f32_e32 v77, v77
	v_pk_mul_f32 v[72:73], v[78:79], v[72:73]
	v_rcp_f32_e32 v206, v206
	v_rcp_f32_e32 v207, v207
	v_pk_mul_f32 v[72:73], v[76:77], v[72:73]
	v_pk_mul_f32 v[74:75], v[206:207], v[74:75]
	v_pk_mul_f32 v[76:77], v[128:129], v[96:97]
	v_pk_mul_f32 v[206:207], v[128:129], v[100:101]
	v_exp_f32_e32 v76, v76
	v_exp_f32_e32 v77, v77
	v_exp_f32_e32 v206, v206
	v_exp_f32_e32 v207, v207
	v_pk_add_f32 v[76:77], v[76:77], 1.0 op_sel_hi:[1,0]
	v_pk_mul_f32 v[78:79], v[130:131], v[96:97]
	v_pk_add_f32 v[206:207], v[206:207], 1.0 op_sel_hi:[1,0]
	v_pk_mul_f32 v[208:209], v[130:131], v[100:101]
	v_rcp_f32_e32 v76, v76
	v_rcp_f32_e32 v77, v77
	v_pk_mul_f32 v[68:69], v[78:79], v[68:69]
	v_rcp_f32_e32 v206, v206
	v_rcp_f32_e32 v207, v207
	v_pk_mul_f32 v[70:71], v[208:209], v[70:71]
	v_pk_mul_f32 v[68:69], v[76:77], v[68:69]
	v_pk_mul_f32 v[70:71], v[206:207], v[70:71]
	v_cvt_pk_fp8_f32 v76, v74, v75
	v_cvt_pk_fp8_f32 v76, v72, v73 op_sel:[0,0,1]
	v_cvt_pk_fp8_f32 v73, v70, v71
	v_add_u32_e32 v70, 0x80, v93
	ds_bpermute_b32 v72, v92, v76
	v_cvt_pk_fp8_f32 v73, v68, v69 op_sel:[0,0,1]
	v_add_u32_e32 v68, 48, v93
	v_mad_i64_i32 v[68:69], s[10:11], v68, s9, v[10:11]
	ds_bpermute_b32 v73, v92, v73
	v_lshl_add_u64 v[68:69], v[68:69], 0, v[0:1]
	s_waitcnt lgkmcnt(0)
	global_store_dwordx2 v[68:69], v[72:73], off
	v_pk_mul_f32 v[68:69], v[128:129], v[64:65]
	v_pk_mul_f32 v[64:65], v[130:131], v[64:65]
	v_exp_f32_e32 v206, v68
	v_exp_f32_e32 v207, v69
	v_pk_mul_f32 v[64:65], v[64:65], v[66:67]
	v_pk_add_f32 v[206:207], v[206:207], 1.0 op_sel_hi:[1,0]
	v_pk_mul_f32 v[66:67], v[128:129], v[62:63]
	v_rcp_f32_e32 v206, v206
	v_rcp_f32_e32 v207, v207
	v_pk_mul_f32 v[62:63], v[130:131], v[62:63]
	v_pk_mul_f32 v[64:65], v[206:207], v[64:65]
	v_pk_mul_f32 v[34:35], v[62:63], v[34:35]
	v_exp_f32_e32 v206, v66
	v_exp_f32_e32 v207, v67
	v_pk_mul_f32 v[62:63], v[128:129], v[60:61]
	v_pk_mul_f32 v[60:61], v[130:131], v[60:61]
	v_pk_add_f32 v[206:207], v[206:207], 1.0 op_sel_hi:[1,0]
	v_pk_mul_f32 v[30:31], v[60:61], v[30:31]
	v_pk_mul_f32 v[60:61], v[128:129], v[58:59]
	v_rcp_f32_e32 v206, v206
	v_rcp_f32_e32 v207, v207
	v_pk_mul_f32 v[58:59], v[130:131], v[58:59]
	v_pk_mul_f32 v[34:35], v[206:207], v[34:35]
	v_pk_mul_f32 v[28:29], v[58:59], v[28:29]
	v_exp_f32_e32 v58, v60
	v_exp_f32_e32 v59, v61
	v_exp_f32_e32 v206, v62
	v_exp_f32_e32 v207, v63
	v_pk_add_f32 v[58:59], v[58:59], 1.0 op_sel_hi:[1,0]
	v_pk_add_f32 v[206:207], v[206:207], 1.0 op_sel_hi:[1,0]
	v_rcp_f32_e32 v58, v58
	v_rcp_f32_e32 v59, v59
	v_rcp_f32_e32 v206, v206
	v_rcp_f32_e32 v207, v207
	v_pk_mul_f32 v[28:29], v[58:59], v[28:29]
	v_pk_mul_f32 v[30:31], v[206:207], v[30:31]
	v_cvt_pk_fp8_f32 v58, v64, v65
	v_cvt_pk_fp8_f32 v58, v34, v35 op_sel:[0,0,1]
	v_cvt_pk_fp8_f32 v35, v30, v31
	v_pk_mul_f32 v[206:207], v[130:131], v[56:57]
	ds_bpermute_b32 v34, v92, v58
	v_pk_mul_f32 v[26:27], v[206:207], v[26:27]
	v_cvt_pk_fp8_f32 v35, v28, v29 op_sel:[0,0,1]
	v_mad_i64_i32 v[28:29], s[10:11], v70, s9, v[10:11]
	v_lshl_add_u64 v[28:29], v[28:29], 0, v[0:1]
	ds_bpermute_b32 v35, v92, v35
	v_pk_mul_f32 v[30:31], v[130:131], v[54:55]
	s_waitcnt lgkmcnt(0)
	global_store_dwordx2 v[28:29], v[34:35], off
	v_pk_mul_f32 v[28:29], v[128:129], v[54:55]
	v_pk_mul_f32 v[206:207], v[128:129], v[56:57]
	v_exp_f32_e32 v28, v28
	v_exp_f32_e32 v29, v29
	v_exp_f32_e32 v206, v206
	v_exp_f32_e32 v207, v207
	v_pk_add_f32 v[28:29], v[28:29], 1.0 op_sel_hi:[1,0]
	v_pk_add_f32 v[206:207], v[206:207], 1.0 op_sel_hi:[1,0]
	v_rcp_f32_e32 v28, v28
	v_rcp_f32_e32 v29, v29
	v_pk_mul_f32 v[24:25], v[30:31], v[24:25]
	v_rcp_f32_e32 v206, v206
	v_rcp_f32_e32 v207, v207
	v_pk_mul_f32 v[24:25], v[28:29], v[24:25]
	v_pk_mul_f32 v[26:27], v[206:207], v[26:27]
	v_pk_mul_f32 v[28:29], v[128:129], v[50:51]
	v_pk_mul_f32 v[206:207], v[128:129], v[52:53]
	v_exp_f32_e32 v28, v28
	v_exp_f32_e32 v29, v29
	v_exp_f32_e32 v206, v206
	v_exp_f32_e32 v207, v207
	v_pk_add_f32 v[28:29], v[28:29], 1.0 op_sel_hi:[1,0]
	v_pk_mul_f32 v[30:31], v[130:131], v[50:51]
	v_pk_add_f32 v[206:207], v[206:207], 1.0 op_sel_hi:[1,0]
	v_pk_mul_f32 v[208:209], v[130:131], v[52:53]
	v_rcp_f32_e32 v28, v28
	v_rcp_f32_e32 v29, v29
	v_pk_mul_f32 v[20:21], v[30:31], v[20:21]
	v_rcp_f32_e32 v206, v206
	v_rcp_f32_e32 v207, v207
	v_pk_mul_f32 v[22:23], v[208:209], v[22:23]
	v_pk_mul_f32 v[20:21], v[28:29], v[20:21]
	v_pk_mul_f32 v[22:23], v[206:207], v[22:23]
	v_cvt_pk_fp8_f32 v28, v26, v27
	v_cvt_pk_fp8_f32 v28, v24, v25 op_sel:[0,0,1]
	v_cvt_pk_fp8_f32 v25, v22, v23
	v_pk_mul_f32 v[206:207], v[130:131], v[48:49]
	ds_bpermute_b32 v24, v92, v28
	v_pk_mul_f32 v[18:19], v[206:207], v[18:19]
	v_cvt_pk_fp8_f32 v25, v20, v21 op_sel:[0,0,1]
	v_add_u32_e32 v20, 0x90, v93
	v_mad_i64_i32 v[20:21], s[10:11], v20, s9, v[10:11]
	ds_bpermute_b32 v25, v92, v25
	v_lshl_add_u64 v[20:21], v[20:21], 0, v[0:1]
	v_pk_mul_f32 v[22:23], v[130:131], v[46:47]
	s_waitcnt lgkmcnt(0)
	global_store_dwordx2 v[20:21], v[24:25], off
	v_pk_mul_f32 v[20:21], v[128:129], v[46:47]
	v_pk_mul_f32 v[206:207], v[128:129], v[48:49]
	v_exp_f32_e32 v20, v20
	v_exp_f32_e32 v21, v21
	v_exp_f32_e32 v206, v206
	v_exp_f32_e32 v207, v207
	v_pk_add_f32 v[20:21], v[20:21], 1.0 op_sel_hi:[1,0]
	v_pk_add_f32 v[206:207], v[206:207], 1.0 op_sel_hi:[1,0]
	v_rcp_f32_e32 v20, v20
	v_rcp_f32_e32 v21, v21
	v_pk_mul_f32 v[16:17], v[22:23], v[16:17]
	v_rcp_f32_e32 v206, v206
	v_rcp_f32_e32 v207, v207
	v_pk_mul_f32 v[16:17], v[20:21], v[16:17]
	v_pk_mul_f32 v[18:19], v[206:207], v[18:19]
	v_pk_mul_f32 v[20:21], v[128:129], v[42:43]
	v_pk_mul_f32 v[206:207], v[128:129], v[44:45]
	v_exp_f32_e32 v20, v20
	v_exp_f32_e32 v21, v21
	v_exp_f32_e32 v206, v206
	v_exp_f32_e32 v207, v207
	v_pk_add_f32 v[20:21], v[20:21], 1.0 op_sel_hi:[1,0]
	v_pk_mul_f32 v[22:23], v[130:131], v[42:43]
	v_pk_add_f32 v[206:207], v[206:207], 1.0 op_sel_hi:[1,0]
	v_pk_mul_f32 v[208:209], v[130:131], v[44:45]
	v_rcp_f32_e32 v20, v20
	v_rcp_f32_e32 v21, v21
	v_pk_mul_f32 v[12:13], v[22:23], v[12:13]
	v_rcp_f32_e32 v206, v206
	v_rcp_f32_e32 v207, v207
	v_pk_mul_f32 v[14:15], v[208:209], v[14:15]
	v_pk_mul_f32 v[12:13], v[20:21], v[12:13]
	v_pk_mul_f32 v[14:15], v[206:207], v[14:15]
	v_cvt_pk_fp8_f32 v20, v18, v19
	v_cvt_pk_fp8_f32 v20, v16, v17 op_sel:[0,0,1]
	v_cvt_pk_fp8_f32 v17, v14, v15
	v_pk_mul_f32 v[206:207], v[130:131], v[40:41]
	ds_bpermute_b32 v16, v92, v20
	v_pk_mul_f32 v[8:9], v[206:207], v[8:9]
	v_cvt_pk_fp8_f32 v17, v12, v13 op_sel:[0,0,1]
	v_add_u32_e32 v12, 0xa0, v93
	v_mad_i64_i32 v[12:13], s[10:11], v12, s9, v[10:11]
	ds_bpermute_b32 v17, v92, v17
	v_lshl_add_u64 v[12:13], v[12:13], 0, v[0:1]
	v_pk_mul_f32 v[14:15], v[130:131], v[38:39]
	s_waitcnt lgkmcnt(0)
	global_store_dwordx2 v[12:13], v[16:17], off
	v_pk_mul_f32 v[12:13], v[128:129], v[38:39]
	v_pk_mul_f32 v[206:207], v[128:129], v[40:41]
	v_exp_f32_e32 v12, v12
	v_exp_f32_e32 v13, v13
	v_exp_f32_e32 v206, v206
	v_exp_f32_e32 v207, v207
	v_pk_add_f32 v[12:13], v[12:13], 1.0 op_sel_hi:[1,0]
	v_pk_add_f32 v[206:207], v[206:207], 1.0 op_sel_hi:[1,0]
	v_rcp_f32_e32 v12, v12
	v_rcp_f32_e32 v13, v13
	v_pk_mul_f32 v[6:7], v[14:15], v[6:7]
	v_rcp_f32_e32 v206, v206
	v_rcp_f32_e32 v207, v207
	v_pk_mul_f32 v[6:7], v[12:13], v[6:7]
	v_pk_mul_f32 v[8:9], v[206:207], v[8:9]
	v_pk_mul_f32 v[12:13], v[128:129], v[32:33]
	v_pk_mul_f32 v[206:207], v[128:129], v[36:37]
	v_exp_f32_e32 v12, v12
	v_exp_f32_e32 v13, v13
	v_exp_f32_e32 v206, v206
	v_exp_f32_e32 v207, v207
	v_pk_add_f32 v[12:13], v[12:13], 1.0 op_sel_hi:[1,0]
	v_pk_mul_f32 v[14:15], v[130:131], v[32:33]
	v_pk_add_f32 v[206:207], v[206:207], 1.0 op_sel_hi:[1,0]
	v_pk_mul_f32 v[208:209], v[130:131], v[36:37]
	v_rcp_f32_e32 v12, v12
	v_rcp_f32_e32 v13, v13
	v_pk_mul_f32 v[2:3], v[14:15], v[2:3]
	v_rcp_f32_e32 v206, v206
	v_rcp_f32_e32 v207, v207
	v_pk_mul_f32 v[4:5], v[208:209], v[4:5]
	v_pk_mul_f32 v[2:3], v[12:13], v[2:3]
	v_pk_mul_f32 v[4:5], v[206:207], v[4:5]
	v_cvt_pk_fp8_f32 v12, v8, v9
	v_cvt_pk_fp8_f32 v12, v6, v7 op_sel:[0,0,1]
	v_cvt_pk_fp8_f32 v7, v4, v5
	ds_bpermute_b32 v6, v92, v12
	v_cvt_pk_fp8_f32 v7, v2, v3 op_sel:[0,0,1]
	v_add_u32_e32 v2, 0xb0, v93
	v_mad_i64_i32 v[2:3], s[10:11], v2, s9, v[10:11]
	ds_bpermute_b32 v7, v92, v7
	v_lshl_add_u64 v[0:1], v[2:3], 0, v[0:1]
	s_waitcnt lgkmcnt(0)
	global_store_dwordx2 v[0:1], v[6:7], off
	s_cbranch_vccnz .LBB0_1303
	s_andn2_b64 vcc, exec, s[20:21]
	s_cbranch_vccnz .LBB0_1302
	s_barrier
	s_branch .LBB0_1302

.LBB0_1472:
	v_cvt_f32_i32_e32 v124, v124
	v_cvt_f32_i32_e32 v125, v125
	v_cvt_f32_i32_e32 v140, v88
	v_cvt_f32_i32_e32 v88, v86
	v_cvt_f32_i32_e32 v86, v80
	v_cvt_f32_i32_e32 v80, v78
	v_cvt_f32_i32_e32 v78, v72
	v_cvt_f32_i32_e32 v72, v70
	v_cvt_f32_i32_e32 v70, v64
	v_cvt_f32_i32_e32 v64, v60
	v_cvt_f32_i32_e32 v60, v56
	v_cvt_f32_i32_e32 v56, v52
	v_cvt_f32_i32_e32 v52, v48
	v_cvt_f32_i32_e32 v48, v44
	v_cvt_f32_i32_e32 v44, v40
	v_cvt_f32_i32_e32 v40, v36
	v_cvt_f32_i32_e32 v36, v32
	v_cvt_f32_i32_e32 v32, v34
	v_cvt_f32_i32_e32 v34, v30
	v_cvt_f32_i32_e32 v30, v24
	v_cvt_f32_i32_e32 v24, v22
	v_cvt_f32_i32_e32 v22, v16
	v_cvt_f32_i32_e32 v16, v14
	v_cvt_f32_i32_e32 v14, v8
	v_cvt_f32_i32_e32 v8, v4
	v_cvt_f32_i32_e32 v4, v0
	v_mbcnt_lo_u32_b32 v0, -1, 0
	v_mbcnt_hi_u32_b32 v0, -1, v0
	s_lshl_b32 s9, s72, 8
	v_cvt_f32_i32_e32 v141, v89
	v_cvt_f32_i32_e32 v89, v87
	v_cvt_f32_i32_e32 v87, v81
	v_cvt_f32_i32_e32 v81, v79
	v_cvt_f32_i32_e32 v79, v73
	v_cvt_f32_i32_e32 v73, v71
	v_cvt_f32_i32_e32 v71, v65
	v_cvt_f32_i32_e32 v65, v61
	v_cvt_f32_i32_e32 v61, v57
	v_cvt_f32_i32_e32 v57, v53
	v_cvt_f32_i32_e32 v53, v49
	v_cvt_f32_i32_e32 v49, v45
	v_cvt_f32_i32_e32 v45, v41
	v_cvt_f32_i32_e32 v41, v37
	v_cvt_f32_i32_e32 v37, v33
	v_cvt_f32_i32_e32 v33, v35
	v_cvt_f32_i32_e32 v35, v31
	v_cvt_f32_i32_e32 v31, v25
	v_cvt_f32_i32_e32 v25, v23
	v_cvt_f32_i32_e32 v23, v17
	v_cvt_f32_i32_e32 v17, v15
	v_cvt_f32_i32_e32 v15, v9
	v_cvt_f32_i32_e32 v9, v5
	v_cvt_f32_i32_e32 v5, v1
	s_add_i32 s9, s9, s36
	v_ashrrev_i32_e32 v1, 2, v0
	v_cvt_f32_i32_e32 v139, v121
	v_cvt_f32_i32_e32 v121, v117
	v_cvt_f32_i32_e32 v117, v113
	v_cvt_f32_i32_e32 v113, v109
	v_cvt_f32_i32_e32 v109, v105
	v_cvt_f32_i32_e32 v105, v101
	v_cvt_f32_i32_e32 v101, v97
	v_cvt_f32_i32_e32 v97, v99
	v_cvt_f32_i32_e32 v99, v93
	v_cvt_f32_i32_e32 v142, v90
	v_cvt_f32_i32_e32 v90, v84
	v_cvt_f32_i32_e32 v84, v82
	v_cvt_f32_i32_e32 v82, v76
	v_cvt_f32_i32_e32 v76, v74
	v_cvt_f32_i32_e32 v74, v68
	v_cvt_f32_i32_e32 v68, v66
	v_cvt_f32_i32_e32 v66, v28
	v_cvt_f32_i32_e32 v28, v26
	v_cvt_f32_i32_e32 v26, v20
	v_cvt_f32_i32_e32 v20, v18
	v_cvt_f32_i32_e32 v18, v12
	v_cvt_f32_i32_e32 v12, v10
	v_and_b32_e32 v10, 3, v0
	v_and_b32_e32 v0, -4, v0
	v_add_u32_e32 v93, s9, v1
	s_lshl_b32 s9, s71, 7
	v_cvt_f32_i32_e32 v138, v120
	v_cvt_f32_i32_e32 v120, v116
	v_cvt_f32_i32_e32 v116, v112
	v_cvt_f32_i32_e32 v112, v108
	v_cvt_f32_i32_e32 v108, v104
	v_cvt_f32_i32_e32 v104, v100
	v_cvt_f32_i32_e32 v100, v96
	v_cvt_f32_i32_e32 v96, v98
	v_cvt_f32_i32_e32 v98, v92
	v_cvt_f32_i32_e32 v143, v91
	v_cvt_f32_i32_e32 v91, v85
	v_cvt_f32_i32_e32 v85, v83
	v_cvt_f32_i32_e32 v83, v77
	v_cvt_f32_i32_e32 v77, v75
	v_cvt_f32_i32_e32 v75, v69
	v_cvt_f32_i32_e32 v69, v67
	v_cvt_f32_i32_e32 v67, v29
	v_cvt_f32_i32_e32 v29, v27
	v_cvt_f32_i32_e32 v27, v21
	v_cvt_f32_i32_e32 v21, v19
	v_cvt_f32_i32_e32 v19, v13
	v_cvt_f32_i32_e32 v13, v11
	v_lshl_add_u32 v92, v10, 6, v0
	v_lshl_or_b32 v0, v10, 3, s9
	v_pk_mul_f32 v[10:11], v[128:129], v[124:125]
	v_cvt_f32_i32_e32 v126, v126
	v_exp_f32_e32 v10, v10
	v_exp_f32_e32 v11, v11
	v_cvt_f32_i32_e32 v127, v127
	v_pk_mul_f32 v[124:125], v[130:131], v[124:125]
	v_cvt_f32_i32_e32 v94, v94
	v_pk_add_f32 v[10:11], v[10:11], 1.0 op_sel_hi:[1,0]
	v_pk_mul_f32 v[98:99], v[124:125], v[98:99]
	v_rcp_f32_e32 v10, v10
	v_rcp_f32_e32 v11, v11
	v_cvt_f32_i32_e32 v95, v95
	v_pk_mul_f32 v[124:125], v[130:131], v[126:127]
	v_cvt_f32_i32_e32 v122, v122
	v_pk_mul_f32 v[10:11], v[10:11], v[98:99]
	v_pk_mul_f32 v[206:207], v[128:129], v[126:127]
	v_pk_mul_f32 v[94:95], v[124:125], v[94:95]
	v_exp_f32_e32 v206, v206
	v_exp_f32_e32 v207, v207
	v_cvt_f32_i32_e32 v123, v123
	v_pk_mul_f32 v[208:209], v[130:131], v[138:139]
	v_or_b32_e32 v0, s37, v0
	v_pk_add_f32 v[206:207], v[206:207], 1.0 op_sel_hi:[1,0]
	v_pk_mul_f32 v[208:209], v[208:209], v[140:141]
	v_rcp_f32_e32 v206, v206
	v_rcp_f32_e32 v207, v207
	s_movk_i32 s9, 0x1600
	v_ashrrev_i32_e32 v1, 31, v0
	v_cvt_f32_i32_e32 v118, v118
	v_pk_mul_f32 v[94:95], v[206:207], v[94:95]
	v_pk_mul_f32 v[98:99], v[128:129], v[138:139]
	v_cvt_f32_i32_e32 v119, v119
	v_exp_f32_e32 v98, v98
	v_exp_f32_e32 v99, v99
	v_cvt_f32_i32_e32 v114, v114
	v_cvt_f32_i32_e32 v115, v115
	v_cvt_f32_i32_e32 v110, v110
	v_pk_add_f32 v[98:99], v[98:99], 1.0 op_sel_hi:[1,0]
	v_cvt_f32_i32_e32 v111, v111
	v_rcp_f32_e32 v98, v98
	v_rcp_f32_e32 v99, v99
	v_cvt_f32_i32_e32 v106, v106
	v_cvt_f32_i32_e32 v107, v107
	v_cvt_f32_i32_e32 v102, v102
	v_pk_mul_f32 v[98:99], v[98:99], v[208:209]
	v_pk_mul_f32 v[124:125], v[128:129], v[122:123]
	v_pk_mul_f32 v[122:123], v[130:131], v[122:123]
	v_exp_f32_e32 v124, v124
	v_exp_f32_e32 v125, v125
	v_pk_mul_f32 v[122:123], v[122:123], v[142:143]
	v_cvt_f32_i32_e32 v103, v103
	v_cvt_f32_i32_e32 v62, v62
	v_pk_add_f32 v[124:125], v[124:125], 1.0 op_sel_hi:[1,0]
	v_cvt_f32_i32_e32 v63, v63
	v_rcp_f32_e32 v124, v124
	v_rcp_f32_e32 v125, v125
	v_cvt_f32_i32_e32 v58, v58
	v_cvt_f32_i32_e32 v59, v59
	v_cvt_f32_i32_e32 v54, v54
	v_pk_mul_f32 v[122:123], v[124:125], v[122:123]
	v_cvt_pk_fp8_f32 v124, v10, v11
	v_cvt_pk_fp8_f32 v10, v98, v99
	v_cvt_f32_i32_e32 v55, v55
	v_cvt_pk_fp8_f32 v124, v94, v95 op_sel:[0,0,1]
	v_cvt_f32_i32_e32 v50, v50
	v_cvt_pk_fp8_f32 v10, v122, v123 op_sel:[0,0,1]
	v_cvt_f32_i32_e32 v51, v51
	ds_bpermute_b32 v94, v92, v124
	v_cvt_f32_i32_e32 v46, v46
	ds_bpermute_b32 v95, v92, v10
	v_mov_b64_e32 v[10:11], s[16:17]
	v_mad_i64_i32 v[98:99], s[10:11], v93, s9, v[10:11]
	v_lshl_add_u64 v[98:99], v[98:99], 0, v[0:1]
	s_waitcnt lgkmcnt(0)
	global_store_dwordx2 v[98:99], v[94:95], off
	v_pk_mul_f32 v[94:95], v[128:129], v[118:119]
	v_pk_mul_f32 v[206:207], v[128:129], v[120:121]
	v_exp_f32_e32 v94, v94
	v_exp_f32_e32 v95, v95
	v_exp_f32_e32 v206, v206
	v_exp_f32_e32 v207, v207
	v_pk_add_f32 v[94:95], v[94:95], 1.0 op_sel_hi:[1,0]
	v_pk_mul_f32 v[98:99], v[130:131], v[118:119]
	v_pk_add_f32 v[206:207], v[206:207], 1.0 op_sel_hi:[1,0]
	v_pk_mul_f32 v[208:209], v[130:131], v[120:121]
	v_rcp_f32_e32 v94, v94
	v_rcp_f32_e32 v95, v95
	v_pk_mul_f32 v[88:89], v[98:99], v[88:89]
	v_rcp_f32_e32 v206, v206
	v_rcp_f32_e32 v207, v207
	v_pk_mul_f32 v[90:91], v[208:209], v[90:91]
	v_pk_mul_f32 v[88:89], v[94:95], v[88:89]
	v_pk_mul_f32 v[90:91], v[206:207], v[90:91]
	v_pk_mul_f32 v[94:95], v[128:129], v[114:115]
	v_pk_mul_f32 v[206:207], v[128:129], v[116:117]
	v_exp_f32_e32 v94, v94
	v_exp_f32_e32 v95, v95
	v_exp_f32_e32 v206, v206
	v_exp_f32_e32 v207, v207
	v_pk_add_f32 v[94:95], v[94:95], 1.0 op_sel_hi:[1,0]
	v_pk_mul_f32 v[98:99], v[130:131], v[114:115]
	v_pk_add_f32 v[206:207], v[206:207], 1.0 op_sel_hi:[1,0]
	v_pk_mul_f32 v[208:209], v[130:131], v[116:117]
	v_rcp_f32_e32 v94, v94
	v_rcp_f32_e32 v95, v95
	v_pk_mul_f32 v[84:85], v[98:99], v[84:85]
	v_rcp_f32_e32 v206, v206
	v_rcp_f32_e32 v207, v207
	v_pk_mul_f32 v[86:87], v[208:209], v[86:87]
	v_pk_mul_f32 v[84:85], v[94:95], v[84:85]
	v_pk_mul_f32 v[86:87], v[206:207], v[86:87]
	v_cvt_pk_fp8_f32 v94, v90, v91
	v_cvt_pk_fp8_f32 v94, v88, v89 op_sel:[0,0,1]
	v_cvt_f32_i32_e32 v47, v47
	v_cvt_f32_i32_e32 v42, v42
	v_cvt_f32_i32_e32 v43, v43
	v_cvt_f32_i32_e32 v38, v38
	v_cvt_f32_i32_e32 v39, v39
	v_cvt_f32_i32_e32 v6, v6
	v_cvt_f32_i32_e32 v7, v7
	v_cvt_f32_i32_e32 v2, v2
	v_cvt_f32_i32_e32 v3, v3
	s_mov_b64 s[48:49], -1
	s_andn2_b64 vcc, exec, s[42:43]
	v_cvt_pk_fp8_f32 v89, v86, v87
	v_pk_mul_f32 v[206:207], v[130:131], v[112:113]
	ds_bpermute_b32 v88, v92, v94
	v_pk_mul_f32 v[82:83], v[206:207], v[82:83]
	v_cvt_pk_fp8_f32 v89, v84, v85 op_sel:[0,0,1]
	v_add_u32_e32 v84, 16, v93
	v_mad_i64_i32 v[84:85], s[10:11], v84, s9, v[10:11]
	ds_bpermute_b32 v89, v92, v89
	v_lshl_add_u64 v[84:85], v[84:85], 0, v[0:1]
	v_pk_mul_f32 v[86:87], v[130:131], v[110:111]
	s_waitcnt lgkmcnt(0)
	global_store_dwordx2 v[84:85], v[88:89], off
	v_pk_mul_f32 v[84:85], v[128:129], v[110:111]
	v_pk_mul_f32 v[206:207], v[128:129], v[112:113]
	v_exp_f32_e32 v84, v84
	v_exp_f32_e32 v85, v85
	v_exp_f32_e32 v206, v206
	v_exp_f32_e32 v207, v207
	v_pk_add_f32 v[84:85], v[84:85], 1.0 op_sel_hi:[1,0]
	v_pk_add_f32 v[206:207], v[206:207], 1.0 op_sel_hi:[1,0]
	v_rcp_f32_e32 v84, v84
	v_rcp_f32_e32 v85, v85
	v_pk_mul_f32 v[80:81], v[86:87], v[80:81]
	v_rcp_f32_e32 v206, v206
	v_rcp_f32_e32 v207, v207
	v_pk_mul_f32 v[80:81], v[84:85], v[80:81]
	v_pk_mul_f32 v[82:83], v[206:207], v[82:83]
	v_pk_mul_f32 v[84:85], v[128:129], v[106:107]
	v_pk_mul_f32 v[206:207], v[128:129], v[108:109]
	v_exp_f32_e32 v84, v84
	v_exp_f32_e32 v85, v85
	v_exp_f32_e32 v206, v206
	v_exp_f32_e32 v207, v207
	v_pk_add_f32 v[84:85], v[84:85], 1.0 op_sel_hi:[1,0]
	v_pk_mul_f32 v[86:87], v[130:131], v[106:107]
	v_pk_add_f32 v[206:207], v[206:207], 1.0 op_sel_hi:[1,0]
	v_pk_mul_f32 v[208:209], v[130:131], v[108:109]
	v_rcp_f32_e32 v84, v84
	v_rcp_f32_e32 v85, v85
	v_pk_mul_f32 v[76:77], v[86:87], v[76:77]
	v_rcp_f32_e32 v206, v206
	v_rcp_f32_e32 v207, v207
	v_pk_mul_f32 v[78:79], v[208:209], v[78:79]
	v_pk_mul_f32 v[76:77], v[84:85], v[76:77]
	v_pk_mul_f32 v[78:79], v[206:207], v[78:79]
	v_cvt_pk_fp8_f32 v84, v82, v83
	v_cvt_pk_fp8_f32 v84, v80, v81 op_sel:[0,0,1]
	v_cvt_pk_fp8_f32 v81, v78, v79
	v_pk_mul_f32 v[206:207], v[130:131], v[104:105]
	ds_bpermute_b32 v80, v92, v84
	v_pk_mul_f32 v[74:75], v[206:207], v[74:75]
	v_cvt_pk_fp8_f32 v81, v76, v77 op_sel:[0,0,1]
	v_add_u32_e32 v76, 32, v93
	v_mad_i64_i32 v[76:77], s[10:11], v76, s9, v[10:11]
	ds_bpermute_b32 v81, v92, v81
	v_lshl_add_u64 v[76:77], v[76:77], 0, v[0:1]
	v_pk_mul_f32 v[78:79], v[130:131], v[102:103]
	s_waitcnt lgkmcnt(0)
	global_store_dwordx2 v[76:77], v[80:81], off
	v_pk_mul_f32 v[76:77], v[128:129], v[102:103]
	v_pk_mul_f32 v[206:207], v[128:129], v[104:105]
	v_exp_f32_e32 v76, v76
	v_exp_f32_e32 v77, v77
	v_exp_f32_e32 v206, v206
	v_exp_f32_e32 v207, v207
	v_pk_add_f32 v[76:77], v[76:77], 1.0 op_sel_hi:[1,0]
	v_pk_add_f32 v[206:207], v[206:207], 1.0 op_sel_hi:[1,0]
	v_rcp_f32_e32 v76, v76
	v_rcp_f32_e32 v77, v77
	v_pk_mul_f32 v[72:73], v[78:79], v[72:73]
	v_rcp_f32_e32 v206, v206
	v_rcp_f32_e32 v207, v207
	v_pk_mul_f32 v[72:73], v[76:77], v[72:73]
	v_pk_mul_f32 v[74:75], v[206:207], v[74:75]
	v_pk_mul_f32 v[76:77], v[128:129], v[96:97]
	v_pk_mul_f32 v[206:207], v[128:129], v[100:101]
	v_exp_f32_e32 v76, v76
	v_exp_f32_e32 v77, v77
	v_exp_f32_e32 v206, v206
	v_exp_f32_e32 v207, v207
	v_pk_add_f32 v[76:77], v[76:77], 1.0 op_sel_hi:[1,0]
	v_pk_mul_f32 v[78:79], v[130:131], v[96:97]
	v_pk_add_f32 v[206:207], v[206:207], 1.0 op_sel_hi:[1,0]
	v_pk_mul_f32 v[208:209], v[130:131], v[100:101]
	v_rcp_f32_e32 v76, v76
	v_rcp_f32_e32 v77, v77
	v_pk_mul_f32 v[68:69], v[78:79], v[68:69]
	v_rcp_f32_e32 v206, v206
	v_rcp_f32_e32 v207, v207
	v_pk_mul_f32 v[70:71], v[208:209], v[70:71]
	v_pk_mul_f32 v[68:69], v[76:77], v[68:69]
	v_pk_mul_f32 v[70:71], v[206:207], v[70:71]
	v_cvt_pk_fp8_f32 v76, v74, v75
	v_cvt_pk_fp8_f32 v76, v72, v73 op_sel:[0,0,1]
	v_cvt_pk_fp8_f32 v73, v70, v71
	v_add_u32_e32 v70, 0x80, v93
	ds_bpermute_b32 v72, v92, v76
	v_cvt_pk_fp8_f32 v73, v68, v69 op_sel:[0,0,1]
	v_add_u32_e32 v68, 48, v93
	v_mad_i64_i32 v[68:69], s[10:11], v68, s9, v[10:11]
	ds_bpermute_b32 v73, v92, v73
	v_lshl_add_u64 v[68:69], v[68:69], 0, v[0:1]
	s_waitcnt lgkmcnt(0)
	global_store_dwordx2 v[68:69], v[72:73], off
	v_pk_mul_f32 v[68:69], v[128:129], v[64:65]
	v_pk_mul_f32 v[64:65], v[130:131], v[64:65]
	v_exp_f32_e32 v206, v68
	v_exp_f32_e32 v207, v69
	v_pk_mul_f32 v[64:65], v[64:65], v[66:67]
	v_pk_add_f32 v[206:207], v[206:207], 1.0 op_sel_hi:[1,0]
	v_pk_mul_f32 v[66:67], v[128:129], v[62:63]
	v_rcp_f32_e32 v206, v206
	v_rcp_f32_e32 v207, v207
	v_pk_mul_f32 v[62:63], v[130:131], v[62:63]
	v_pk_mul_f32 v[64:65], v[206:207], v[64:65]
	v_pk_mul_f32 v[34:35], v[62:63], v[34:35]
	v_exp_f32_e32 v206, v66
	v_exp_f32_e32 v207, v67
	v_pk_mul_f32 v[62:63], v[128:129], v[60:61]
	v_pk_mul_f32 v[60:61], v[130:131], v[60:61]
	v_pk_add_f32 v[206:207], v[206:207], 1.0 op_sel_hi:[1,0]
	v_pk_mul_f32 v[30:31], v[60:61], v[30:31]
	v_pk_mul_f32 v[60:61], v[128:129], v[58:59]
	v_rcp_f32_e32 v206, v206
	v_rcp_f32_e32 v207, v207
	v_pk_mul_f32 v[58:59], v[130:131], v[58:59]
	v_pk_mul_f32 v[34:35], v[206:207], v[34:35]
	v_pk_mul_f32 v[28:29], v[58:59], v[28:29]
	v_exp_f32_e32 v58, v60
	v_exp_f32_e32 v59, v61
	v_exp_f32_e32 v206, v62
	v_exp_f32_e32 v207, v63
	v_pk_add_f32 v[58:59], v[58:59], 1.0 op_sel_hi:[1,0]
	v_pk_add_f32 v[206:207], v[206:207], 1.0 op_sel_hi:[1,0]
	v_rcp_f32_e32 v58, v58
	v_rcp_f32_e32 v59, v59
	v_rcp_f32_e32 v206, v206
	v_rcp_f32_e32 v207, v207
	v_pk_mul_f32 v[28:29], v[58:59], v[28:29]
	v_pk_mul_f32 v[30:31], v[206:207], v[30:31]
	v_cvt_pk_fp8_f32 v58, v64, v65
	v_cvt_pk_fp8_f32 v58, v34, v35 op_sel:[0,0,1]
	v_cvt_pk_fp8_f32 v35, v30, v31
	v_pk_mul_f32 v[206:207], v[130:131], v[56:57]
	ds_bpermute_b32 v34, v92, v58
	v_pk_mul_f32 v[26:27], v[206:207], v[26:27]
	v_cvt_pk_fp8_f32 v35, v28, v29 op_sel:[0,0,1]
	v_mad_i64_i32 v[28:29], s[10:11], v70, s9, v[10:11]
	v_lshl_add_u64 v[28:29], v[28:29], 0, v[0:1]
	ds_bpermute_b32 v35, v92, v35
	v_pk_mul_f32 v[30:31], v[130:131], v[54:55]
	s_waitcnt lgkmcnt(0)
	global_store_dwordx2 v[28:29], v[34:35], off
	v_pk_mul_f32 v[28:29], v[128:129], v[54:55]
	v_pk_mul_f32 v[206:207], v[128:129], v[56:57]
	v_exp_f32_e32 v28, v28
	v_exp_f32_e32 v29, v29
	v_exp_f32_e32 v206, v206
	v_exp_f32_e32 v207, v207
	v_pk_add_f32 v[28:29], v[28:29], 1.0 op_sel_hi:[1,0]
	v_pk_add_f32 v[206:207], v[206:207], 1.0 op_sel_hi:[1,0]
	v_rcp_f32_e32 v28, v28
	v_rcp_f32_e32 v29, v29
	v_pk_mul_f32 v[24:25], v[30:31], v[24:25]
	v_rcp_f32_e32 v206, v206
	v_rcp_f32_e32 v207, v207
	v_pk_mul_f32 v[24:25], v[28:29], v[24:25]
	v_pk_mul_f32 v[26:27], v[206:207], v[26:27]
	v_pk_mul_f32 v[28:29], v[128:129], v[50:51]
	v_pk_mul_f32 v[206:207], v[128:129], v[52:53]
	v_exp_f32_e32 v28, v28
	v_exp_f32_e32 v29, v29
	v_exp_f32_e32 v206, v206
	v_exp_f32_e32 v207, v207
	v_pk_add_f32 v[28:29], v[28:29], 1.0 op_sel_hi:[1,0]
	v_pk_mul_f32 v[30:31], v[130:131], v[50:51]
	v_pk_add_f32 v[206:207], v[206:207], 1.0 op_sel_hi:[1,0]
	v_pk_mul_f32 v[208:209], v[130:131], v[52:53]
	v_rcp_f32_e32 v28, v28
	v_rcp_f32_e32 v29, v29
	v_pk_mul_f32 v[20:21], v[30:31], v[20:21]
	v_rcp_f32_e32 v206, v206
	v_rcp_f32_e32 v207, v207
	v_pk_mul_f32 v[22:23], v[208:209], v[22:23]
	v_pk_mul_f32 v[20:21], v[28:29], v[20:21]
	v_pk_mul_f32 v[22:23], v[206:207], v[22:23]
	v_cvt_pk_fp8_f32 v28, v26, v27
	v_cvt_pk_fp8_f32 v28, v24, v25 op_sel:[0,0,1]
	v_cvt_pk_fp8_f32 v25, v22, v23
	v_pk_mul_f32 v[206:207], v[130:131], v[48:49]
	ds_bpermute_b32 v24, v92, v28
	v_pk_mul_f32 v[18:19], v[206:207], v[18:19]
	v_cvt_pk_fp8_f32 v25, v20, v21 op_sel:[0,0,1]
	v_add_u32_e32 v20, 0x90, v93
	v_mad_i64_i32 v[20:21], s[10:11], v20, s9, v[10:11]
	ds_bpermute_b32 v25, v92, v25
	v_lshl_add_u64 v[20:21], v[20:21], 0, v[0:1]
	v_pk_mul_f32 v[22:23], v[130:131], v[46:47]
	s_waitcnt lgkmcnt(0)
	global_store_dwordx2 v[20:21], v[24:25], off
	v_pk_mul_f32 v[20:21], v[128:129], v[46:47]
	v_pk_mul_f32 v[206:207], v[128:129], v[48:49]
	v_exp_f32_e32 v20, v20
	v_exp_f32_e32 v21, v21
	v_exp_f32_e32 v206, v206
	v_exp_f32_e32 v207, v207
	v_pk_add_f32 v[20:21], v[20:21], 1.0 op_sel_hi:[1,0]
	v_pk_add_f32 v[206:207], v[206:207], 1.0 op_sel_hi:[1,0]
	v_rcp_f32_e32 v20, v20
	v_rcp_f32_e32 v21, v21
	v_pk_mul_f32 v[16:17], v[22:23], v[16:17]
	v_rcp_f32_e32 v206, v206
	v_rcp_f32_e32 v207, v207
	v_pk_mul_f32 v[16:17], v[20:21], v[16:17]
	v_pk_mul_f32 v[18:19], v[206:207], v[18:19]
	v_pk_mul_f32 v[20:21], v[128:129], v[42:43]
	v_pk_mul_f32 v[206:207], v[128:129], v[44:45]
	v_exp_f32_e32 v20, v20
	v_exp_f32_e32 v21, v21
	v_exp_f32_e32 v206, v206
	v_exp_f32_e32 v207, v207
	v_pk_add_f32 v[20:21], v[20:21], 1.0 op_sel_hi:[1,0]
	v_pk_mul_f32 v[22:23], v[130:131], v[42:43]
	v_pk_add_f32 v[206:207], v[206:207], 1.0 op_sel_hi:[1,0]
	v_pk_mul_f32 v[208:209], v[130:131], v[44:45]
	v_rcp_f32_e32 v20, v20
	v_rcp_f32_e32 v21, v21
	v_pk_mul_f32 v[12:13], v[22:23], v[12:13]
	v_rcp_f32_e32 v206, v206
	v_rcp_f32_e32 v207, v207
	v_pk_mul_f32 v[14:15], v[208:209], v[14:15]
	v_pk_mul_f32 v[12:13], v[20:21], v[12:13]
	v_pk_mul_f32 v[14:15], v[206:207], v[14:15]
	v_cvt_pk_fp8_f32 v20, v18, v19
	v_cvt_pk_fp8_f32 v20, v16, v17 op_sel:[0,0,1]
	v_cvt_pk_fp8_f32 v17, v14, v15
	v_pk_mul_f32 v[206:207], v[130:131], v[40:41]
	ds_bpermute_b32 v16, v92, v20
	v_pk_mul_f32 v[8:9], v[206:207], v[8:9]
	v_cvt_pk_fp8_f32 v17, v12, v13 op_sel:[0,0,1]
	v_add_u32_e32 v12, 0xa0, v93
	v_mad_i64_i32 v[12:13], s[10:11], v12, s9, v[10:11]
	ds_bpermute_b32 v17, v92, v17
	v_lshl_add_u64 v[12:13], v[12:13], 0, v[0:1]
	v_pk_mul_f32 v[14:15], v[130:131], v[38:39]
	s_waitcnt lgkmcnt(0)
	global_store_dwordx2 v[12:13], v[16:17], off
	v_pk_mul_f32 v[12:13], v[128:129], v[38:39]
	v_pk_mul_f32 v[206:207], v[128:129], v[40:41]
	v_exp_f32_e32 v12, v12
	v_exp_f32_e32 v13, v13
	v_exp_f32_e32 v206, v206
	v_exp_f32_e32 v207, v207
	v_pk_add_f32 v[12:13], v[12:13], 1.0 op_sel_hi:[1,0]
	v_pk_add_f32 v[206:207], v[206:207], 1.0 op_sel_hi:[1,0]
	v_rcp_f32_e32 v12, v12
	v_rcp_f32_e32 v13, v13
	v_pk_mul_f32 v[6:7], v[14:15], v[6:7]
	v_rcp_f32_e32 v206, v206
	v_rcp_f32_e32 v207, v207
	v_pk_mul_f32 v[6:7], v[12:13], v[6:7]
	v_pk_mul_f32 v[8:9], v[206:207], v[8:9]
	v_pk_mul_f32 v[12:13], v[128:129], v[32:33]
	v_pk_mul_f32 v[206:207], v[128:129], v[36:37]
	v_exp_f32_e32 v12, v12
	v_exp_f32_e32 v13, v13
	v_exp_f32_e32 v206, v206
	v_exp_f32_e32 v207, v207
	v_pk_add_f32 v[12:13], v[12:13], 1.0 op_sel_hi:[1,0]
	v_pk_mul_f32 v[14:15], v[130:131], v[32:33]
	v_pk_add_f32 v[206:207], v[206:207], 1.0 op_sel_hi:[1,0]
	v_pk_mul_f32 v[208:209], v[130:131], v[36:37]
	v_rcp_f32_e32 v12, v12
	v_rcp_f32_e32 v13, v13
	v_pk_mul_f32 v[2:3], v[14:15], v[2:3]
	v_rcp_f32_e32 v206, v206
	v_rcp_f32_e32 v207, v207
	v_pk_mul_f32 v[4:5], v[208:209], v[4:5]
	v_pk_mul_f32 v[2:3], v[12:13], v[2:3]
	v_pk_mul_f32 v[4:5], v[206:207], v[4:5]
	v_cvt_pk_fp8_f32 v12, v8, v9
	v_cvt_pk_fp8_f32 v12, v6, v7 op_sel:[0,0,1]
	v_cvt_pk_fp8_f32 v7, v4, v5
	ds_bpermute_b32 v6, v92, v12
	v_cvt_pk_fp8_f32 v7, v2, v3 op_sel:[0,0,1]
	v_add_u32_e32 v2, 0xb0, v93
	v_mad_i64_i32 v[2:3], s[10:11], v2, s9, v[10:11]
	ds_bpermute_b32 v7, v92, v7
	v_lshl_add_u64 v[0:1], v[2:3], 0, v[0:1]
	s_waitcnt lgkmcnt(0)
	global_store_dwordx2 v[0:1], v[6:7], off
	s_cbranch_vccnz .LBB0_1465
	s_andn2_b64 vcc, exec, s[0:1]
	s_cbranch_vccnz .LBB0_1464
	s_barrier
	s_branch .LBB0_1464
